# PEER tail round on waves 0 and 2 (two non-adjacent SIMDs, both at default priority)
# speedup vs baseline: 1.0029x; 1.0029x over previous
.LBB0_719:
	s_lshl_b32 s6, s33, 3
	s_add_i32 s6, s6, s88
	s_cmpk_lt_i32 s6, 0x4000
	s_cbranch_scc1 .Lpe_notail
	s_cmpk_lg_u32 s33, 0x100
	s_cbranch_scc1 .Lpe_notail
	s_and_b32 s8, s6, 7
	s_and_b32 s74, s8, 5
	s_lshr_b32 s8, s8, 1
	s_sub_i32 s9, s6, 0x4000
	s_lshr_b32 s9, s9, 3
	s_lshl_b32 s9, s9, 1
	s_add_i32 s9, s9, s8
	s_addk_i32 s9, 0x4000
	s_cmp_eq_u32 s74, 0
	s_cselect_b32 s6, s9, 0x7ffffff0
